# P6c: non-temporal hint on the eight read-once partial-row loads
# baseline (speedup 1.0000x reference)
; __device__ __forceinline__ void row_peer_reduce(const Params& P, unsigned char* ws, int l, int rowi, int lane, float* __restrict__ xout) {
;     const size_t n = (size_t)rowi; const bf16* Z = (const bf16*)(ws + WS_Z); const unsigned char* PARTQ = ws + WS_PART; const float* PSCL = (const float*)(ws + WS_PSCL);
;     const f2 st = *(const f2*)((const float*)(ws + WS_X1) + 2 * n);
;     const float* g1 = P.in[16] + (size_t)l * D; const float* b1 = P.in[17] + (size_t)l * D;
;     float acc[32];
; #pragma unroll
;     for (int j = 0; j < 2; ++j)
; #pragma unroll
;         for (int q = 0; q < 4; ++q) { const int col = 1024 * j + 16 * lane + 4 * q; const u2 zw = *(const u2*)(Z + n * D + col); const f4 a = mk_f4(__uint_as_float(zw.x << 16), __uint_as_float(zw.x & 0xffff0000u), __uint_as_float(zw.y << 16), __uint_as_float(zw.y & 0xffff0000u)), gg = *(const f4*)(g1 + col), bb = *(const f4*)(b1 + col);
;             acc[16 * j + 4 * q] = ALPHA * ((a.x - st.x) * st.y * gg.x + bb.x); acc[16 * j + 4 * q + 1] = ALPHA * ((a.y - st.x) * st.y * gg.y + bb.y);
;             acc[16 * j + 4 * q + 2] = ALPHA * ((a.z - st.x) * st.y * gg.z + bb.z); acc[16 * j + 4 * q + 3] = ALPHA * ((a.w - st.x) * st.y * gg.w + bb.w); }
; #pragma unroll 4
;     for (int xb_ = 0; xb_ < 8; ++xb_) { const u4 a = *(const u4*)(PARTQ + ((size_t)xb_ * NTOK + ((n + 5u * (unsigned)xb_) & (size_t)(NTOK - 1))) * 1024u + (unsigned)(16 * lane)); const float psc = PSCL[(size_t)xb_ * NTOK + n];
.LBB0_1592:
	s_add_u32 s26, s92, 0x5b000000
	s_addc_u32 s27, s93, 0
	s_add_u32 s28, s92, 0x64000000
	s_addc_u32 s29, s93, 0
	s_and_b32 s22, s6, 0x1fff
	s_lshl_b32 s22, s22, 10
	v_add_u32_e32 v144, s22, v32
	global_load_dwordx4 v[104:107], v144, s[26:27] nt
	s_lshl_b32 s23, s6, 2
	v_mov_b32_e32 v176, s23
	global_load_dword v136, v176, s[28:29]
	s_add_i32 s22, s6, 5
	s_and_b32 s22, s22, 0x1fff
	s_lshl_b32 s22, s22, 10
	s_add_i32 s22, s22, 0x800000
	v_add_u32_e32 v145, s22, v32
	global_load_dwordx4 v[108:111], v145, s[26:27] nt
	s_add_i32 s23, s6, 0x2000
	s_lshl_b32 s23, s23, 2
	v_mov_b32_e32 v177, s23
	global_load_dword v137, v177, s[28:29]
	s_add_i32 s22, s6, 10
	s_and_b32 s22, s22, 0x1fff
	s_lshl_b32 s22, s22, 10
	s_add_i32 s22, s22, 0x1000000
	v_add_u32_e32 v146, s22, v32
	global_load_dwordx4 v[112:115], v146, s[26:27] nt
	s_add_i32 s23, s6, 0x4000
	s_lshl_b32 s23, s23, 2
	v_mov_b32_e32 v178, s23
	global_load_dword v138, v178, s[28:29]
	s_add_i32 s22, s6, 15
	s_and_b32 s22, s22, 0x1fff
	s_lshl_b32 s22, s22, 10
	s_add_i32 s22, s22, 0x1800000
	v_add_u32_e32 v147, s22, v32
	global_load_dwordx4 v[116:119], v147, s[26:27] nt
	s_add_i32 s23, s6, 0x6000
	s_lshl_b32 s23, s23, 2
	v_mov_b32_e32 v179, s23
	global_load_dword v139, v179, s[28:29]
	s_add_i32 s22, s6, 20
	s_and_b32 s22, s22, 0x1fff
	s_lshl_b32 s22, s22, 10
	s_add_i32 s22, s22, 0x2000000
	v_add_u32_e32 v148, s22, v32
	global_load_dwordx4 v[120:123], v148, s[26:27] nt
	s_add_i32 s23, s6, 0x8000
	s_lshl_b32 s23, s23, 2
	v_mov_b32_e32 v180, s23
	global_load_dword v140, v180, s[28:29]
	s_add_i32 s22, s6, 25
	s_and_b32 s22, s22, 0x1fff
	s_lshl_b32 s22, s22, 10
	s_add_i32 s22, s22, 0x2800000
	v_add_u32_e32 v149, s22, v32
	global_load_dwordx4 v[124:127], v149, s[26:27] nt
	s_add_i32 s23, s6, 0xa000
	s_lshl_b32 s23, s23, 2
	v_mov_b32_e32 v181, s23
	global_load_dword v141, v181, s[28:29]
	s_add_i32 s22, s6, 30
	s_and_b32 s22, s22, 0x1fff
	s_lshl_b32 s22, s22, 10
	s_add_i32 s22, s22, 0x3000000
	v_add_u32_e32 v150, s22, v32
	global_load_dwordx4 v[128:131], v150, s[26:27] nt
	s_add_i32 s23, s6, 0xc000
	s_lshl_b32 s23, s23, 2
	v_mov_b32_e32 v182, s23
	global_load_dword v142, v182, s[28:29]
	s_add_i32 s22, s6, 35
	s_and_b32 s22, s22, 0x1fff
	s_lshl_b32 s22, s22, 10
	s_add_i32 s22, s22, 0x3800000
	v_add_u32_e32 v151, s22, v32
	global_load_dwordx4 v[132:135], v151, s[26:27] nt
	s_add_i32 s23, s6, 0xe000
	s_lshl_b32 s23, s23, 2
	v_mov_b32_e32 v183, s23
	global_load_dword v143, v183, s[28:29]
	s_ashr_i32 s7, s6, 31
	s_lshl_b64 s[4:5], s[6:7], 3
	s_add_u32 s4, s38, s4
	s_addc_u32 s5, s39, s5
	global_load_dwordx2 v[74:75], v80, s[4:5]
	s_lshl_b64 s[12:13], s[6:7], 12
	v_lshl_add_u64 v[4:5], v[52:53], 0, s[12:13]
	global_load_dwordx4 v[0:3], v[4:5], off offset:16
	global_load_dwordx4 v[6:9], v[4:5], off
	global_load_dwordx4 v[184:187], v[4:5], off offset:2064
	global_load_dwordx4 v[188:191], v[4:5], off offset:2048
	global_load_dwordx4 v[10:13], v[34:35], off offset:48
	global_load_dwordx4 v[14:17], v[34:35], off offset:32
	global_load_dwordx4 v[18:21], v[34:35], off offset:16
	global_load_dwordx4 v[22:25], v[34:35], off
	global_load_dwordx4 v[26:29], v[36:37], off offset:48
	global_load_dwordx4 v[64:67], v[36:37], off offset:32
	global_load_dwordx4 v[60:63], v[36:37], off offset:16
	global_load_dwordx4 v[56:59], v[36:37], off
	s_mov_b32 s4, 0x3fd744fd
	s_mov_b64 s[14:15], 0x4000
	s_mov_b64 s[16:17], 0x2000
	s_mov_b64 s[18:19], 0
	s_mov_b32 s47, s46
	s_mov_b32 s48, s45
	s_mov_b32 s49, s44
	s_mov_b32 s50, s43
	s_mov_b64 s[34:35], 0
	s_waitcnt vmcnt(0)
; __device__ __forceinline__ void row_peer_reduce(const Params& P, unsigned char* ws, int l, int rowi, int lane, float* __restrict__ xout) {
;     ...
;     for (int j = 0; j < 2; ++j)
; #pragma unroll
;         for (int q = 0; q < 4; ++q) { const int col = 1024 * j + 16 * lane + 4 * q; const u2 zw = *(const u2*)(Z + n * D + col); const f4 a = mk_f4(__uint_as_float(zw.x << 16), __uint_as_float(zw.x & 0xffff0000u), __uint_as_float(zw.y << 16), __uint_as_float(zw.y & 0xffff0000u)), gg = *(const f4*)(g1 + col), bb = *(const f4*)(b1 + col);
;             acc[16 * j + 4 * q] = ALPHA * ((a.x - st.x) * st.y * gg.x + bb.x); acc[16 * j + 4 * q + 1] = ALPHA * ((a.y - st.x) * st.y * gg.y + bb.y);
;             acc[16 * j + 4 * q + 2] = ALPHA * ((a.z - st.x) * st.y * gg.z + bb.z); acc[16 * j + 4 * q + 3] = ALPHA * ((a.w - st.x) * st.y * gg.w + bb.w); }
	v_lshlrev_b32_e32 v30, 16, v6
	v_and_b32_e32 v31, 0xffff0000, v6
	v_lshlrev_b32_e32 v6, 16, v7
	v_and_b32_e32 v7, 0xffff0000, v7
	v_pk_add_f32 v[6:7], v[6:7], v[74:75] op_sel_hi:[1,0] neg_lo:[0,1] neg_hi:[0,1]
	s_nop 0
	v_pk_mul_f32 v[6:7], v[74:75], v[6:7] op_sel:[1,0]
	v_pk_add_f32 v[30:31], v[30:31], v[74:75] op_sel_hi:[1,0] neg_lo:[0,1] neg_hi:[0,1]
	v_pk_fma_f32 v[6:7], v[24:25], v[6:7], v[58:59]
	v_pk_mul_f32 v[30:31], v[74:75], v[30:31] op_sel:[1,0]
	v_pk_mul_f32 v[58:59], v[6:7], s[4:5] op_sel_hi:[1,0]
	v_lshlrev_b32_e32 v6, 16, v8
	v_and_b32_e32 v7, 0xffff0000, v8
	v_pk_add_f32 v[6:7], v[6:7], v[74:75] op_sel_hi:[1,0] neg_lo:[0,1] neg_hi:[0,1]
	v_pk_fma_f32 v[22:23], v[22:23], v[30:31], v[56:57]
	v_pk_mul_f32 v[6:7], v[74:75], v[6:7] op_sel:[1,0]
	v_pk_mul_f32 v[56:57], v[22:23], s[4:5] op_sel_hi:[1,0]
	v_pk_fma_f32 v[6:7], v[18:19], v[6:7], v[60:61]
	s_nop 0
	v_pk_mul_f32 v[60:61], v[6:7], s[4:5] op_sel_hi:[1,0]
	v_lshlrev_b32_e32 v6, 16, v9
	v_and_b32_e32 v7, 0xffff0000, v9
	v_pk_add_f32 v[6:7], v[6:7], v[74:75] op_sel_hi:[1,0] neg_lo:[0,1] neg_hi:[0,1]
	s_nop 0
	v_pk_mul_f32 v[6:7], v[74:75], v[6:7] op_sel:[1,0]
	s_nop 0
	v_pk_fma_f32 v[6:7], v[20:21], v[6:7], v[62:63]
	s_nop 0
	v_pk_mul_f32 v[62:63], v[6:7], s[4:5] op_sel_hi:[1,0]
	v_lshlrev_b32_e32 v6, 16, v0
	v_and_b32_e32 v7, 0xffff0000, v0
	v_lshlrev_b32_e32 v0, 16, v1
	v_and_b32_e32 v1, 0xffff0000, v1
	v_pk_add_f32 v[0:1], v[0:1], v[74:75] op_sel_hi:[1,0] neg_lo:[0,1] neg_hi:[0,1]
	v_pk_add_f32 v[6:7], v[6:7], v[74:75] op_sel_hi:[1,0] neg_lo:[0,1] neg_hi:[0,1]
	v_pk_mul_f32 v[0:1], v[74:75], v[0:1] op_sel:[1,0]
	v_pk_mul_f32 v[6:7], v[74:75], v[6:7] op_sel:[1,0]
	v_pk_fma_f32 v[0:1], v[16:17], v[0:1], v[66:67]
	v_pk_fma_f32 v[6:7], v[14:15], v[6:7], v[64:65]
	v_pk_mul_f32 v[66:67], v[0:1], s[4:5] op_sel_hi:[1,0]
	v_lshlrev_b32_e32 v0, 16, v2
	v_and_b32_e32 v1, 0xffff0000, v2
	v_pk_add_f32 v[0:1], v[0:1], v[74:75] op_sel_hi:[1,0] neg_lo:[0,1] neg_hi:[0,1]
	v_pk_mul_f32 v[64:65], v[6:7], s[4:5] op_sel_hi:[1,0]
	v_pk_mul_f32 v[0:1], v[74:75], v[0:1] op_sel:[1,0]
	s_nop 0
	v_pk_fma_f32 v[0:1], v[10:11], v[0:1], v[26:27]
	s_nop 0
	v_pk_mul_f32 v[68:69], v[0:1], s[4:5] op_sel_hi:[1,0]
	v_lshlrev_b32_e32 v0, 16, v3
	v_and_b32_e32 v1, 0xffff0000, v3
	v_pk_add_f32 v[0:1], v[0:1], v[74:75] op_sel_hi:[1,0] neg_lo:[0,1] neg_hi:[0,1]
	s_nop 0
	v_pk_mul_f32 v[0:1], v[74:75], v[0:1] op_sel:[1,0]
	s_nop 0
	v_pk_fma_f32 v[0:1], v[12:13], v[0:1], v[28:29]
	s_nop 0
	v_pk_mul_f32 v[70:71], v[0:1], s[4:5] op_sel_hi:[1,0]
	v_mov_b64_e32 v[0:1], v[184:185]
	v_mov_b64_e32 v[2:3], v[186:187]
	v_mov_b64_e32 v[28:29], v[188:189]
	v_mov_b64_e32 v[30:31], v[190:191]
	s_nop 0
	global_load_dwordx4 v[4:7], v[38:39], off offset:48
	global_load_dwordx4 v[12:15], v[38:39], off offset:32
	global_load_dwordx4 v[20:23], v[38:39], off offset:16
	global_load_dwordx4 v[82:85], v[38:39], off
	global_load_dwordx4 v[8:11], v[40:41], off offset:48
	global_load_dwordx4 v[16:19], v[40:41], off offset:32
	global_load_dwordx4 v[24:27], v[40:41], off offset:16
	global_load_dwordx4 v[86:89], v[40:41], off
	s_waitcnt vmcnt(8)
	v_lshlrev_b32_e32 v72, 16, v28
	v_and_b32_e32 v73, 0xffff0000, v28
	v_pk_add_f32 v[72:73], v[72:73], v[74:75] op_sel_hi:[1,0] neg_lo:[0,1] neg_hi:[0,1]
	v_lshlrev_b32_e32 v28, 16, v29
	v_pk_mul_f32 v[72:73], v[74:75], v[72:73] op_sel:[1,0]
	v_and_b32_e32 v29, 0xffff0000, v29
	v_pk_add_f32 v[28:29], v[28:29], v[74:75] op_sel_hi:[1,0] neg_lo:[0,1] neg_hi:[0,1]
	s_waitcnt vmcnt(0)
	v_pk_fma_f32 v[72:73], v[82:83], v[72:73], v[86:87]
	v_lshlrev_b32_e32 v82, 16, v30
	v_and_b32_e32 v83, 0xffff0000, v30
	v_pk_add_f32 v[82:83], v[82:83], v[74:75] op_sel_hi:[1,0] neg_lo:[0,1] neg_hi:[0,1]
	v_pk_mul_f32 v[28:29], v[74:75], v[28:29] op_sel:[1,0]
	v_pk_mul_f32 v[82:83], v[74:75], v[82:83] op_sel:[1,0]
	v_pk_fma_f32 v[28:29], v[84:85], v[28:29], v[88:89]
	v_pk_fma_f32 v[20:21], v[20:21], v[82:83], v[24:25]
	v_lshlrev_b32_e32 v24, 16, v31
	v_and_b32_e32 v25, 0xffff0000, v31
	v_pk_add_f32 v[24:25], v[24:25], v[74:75] op_sel_hi:[1,0] neg_lo:[0,1] neg_hi:[0,1]
	v_pk_mul_f32 v[72:73], v[72:73], s[4:5] op_sel_hi:[1,0]
	v_pk_mul_f32 v[24:25], v[74:75], v[24:25] op_sel:[1,0]
	v_pk_mul_f32 v[28:29], v[28:29], s[4:5] op_sel_hi:[1,0]
	v_pk_fma_f32 v[22:23], v[22:23], v[24:25], v[26:27]
	v_lshlrev_b32_e32 v24, 16, v0
	v_and_b32_e32 v25, 0xffff0000, v0
	v_lshlrev_b32_e32 v0, 16, v1
	v_and_b32_e32 v1, 0xffff0000, v1
	v_pk_add_f32 v[0:1], v[0:1], v[74:75] op_sel_hi:[1,0] neg_lo:[0,1] neg_hi:[0,1]
	v_pk_add_f32 v[24:25], v[24:25], v[74:75] op_sel_hi:[1,0] neg_lo:[0,1] neg_hi:[0,1]
	v_pk_mul_f32 v[0:1], v[74:75], v[0:1] op_sel:[1,0]
	v_pk_mul_f32 v[24:25], v[74:75], v[24:25] op_sel:[1,0]
	v_pk_fma_f32 v[0:1], v[14:15], v[0:1], v[18:19]
	v_lshlrev_b32_e32 v14, 16, v2
	v_and_b32_e32 v15, 0xffff0000, v2
	v_lshlrev_b32_e32 v2, 16, v3
	v_and_b32_e32 v3, 0xffff0000, v3
	v_pk_add_f32 v[14:15], v[14:15], v[74:75] op_sel_hi:[1,0] neg_lo:[0,1] neg_hi:[0,1]
	v_pk_add_f32 v[2:3], v[2:3], v[74:75] op_sel_hi:[1,0] neg_lo:[0,1] neg_hi:[0,1]
	v_pk_mul_f32 v[14:15], v[74:75], v[14:15] op_sel:[1,0]
	v_pk_mul_f32 v[2:3], v[74:75], v[2:3] op_sel:[1,0]
	v_pk_fma_f32 v[12:13], v[12:13], v[24:25], v[16:17]
	v_pk_fma_f32 v[4:5], v[4:5], v[14:15], v[8:9]
	v_pk_fma_f32 v[2:3], v[6:7], v[2:3], v[10:11]
	v_pk_mul_f32 v[20:21], v[20:21], s[4:5] op_sel_hi:[1,0]
	v_pk_mul_f32 v[22:23], v[22:23], s[4:5] op_sel_hi:[1,0]
	v_pk_mul_f32 v[12:13], v[12:13], s[4:5] op_sel_hi:[1,0]
	v_pk_mul_f32 v[0:1], v[0:1], s[4:5] op_sel_hi:[1,0]
	v_pk_mul_f32 v[4:5], v[4:5], s[4:5] op_sel_hi:[1,0]
	v_pk_mul_f32 v[2:3], v[2:3], s[4:5] op_sel_hi:[1,0]
	s_mov_b64 s[4:5], 0x6000
